# stacked+fold + attention block epilogues: output normalization multiplies packed (v_pk_mul_f32), 32 fewer VALU per block
# speedup vs baseline: 1.0008x; 1.0008x over previous
.LBB0_635:
	s_waitcnt vmcnt(8)
	s_waitcnt vmcnt(9)
	ds_write_b128 v221, v[98:101] offset:32768
	s_waitcnt vmcnt(8)
	ds_write_b128 v221, v[102:105] offset:40960
	s_and_saveexec_b64 s[8:9], s[4:5]
	ds_write_b32 v223, v114
	s_or_b64 exec, exec, s[8:9]
	s_waitcnt lgkmcnt(0)
	ds_read_b128 v[66:69], v205
	ds_read_b128 v[70:73], v205 offset:32
	ds_read_b128 v[74:77], v205 offset:64
	ds_read_b128 v[78:81], v205 offset:96
	s_add_u32 s0, s22, s24
	s_addc_u32 s1, s23, s25
	s_lshl_b32 s2, s43, 12
	s_add_u32 s0, s0, s2
	s_addc_u32 s1, s1, 0
	v_lshrrev_b32_e32 v82, 6, v254
	v_lshlrev_b32_e32 v82, 13, v82
	v_add_u32_e32 v82, 0x11000, v82
	v_and_b32_e32 v83, 31, v213
	v_lshrrev_b32_e32 v84, 5, v213
	v_lshlrev_b32_e32 v83, 1, v83
	v_lshl_add_u32 v83, v84, 10, v83
	v_add_u32_e32 v83, v82, v83
	v_lshl_add_u32 v82, v213, 4, v82
	v_lshrrev_b32_e32 v84, 4, v213
	v_and_b32_e32 v85, 15, v213
	v_lshlrev_b32_e32 v85, 4, v85
	v_lshl_add_u32 v84, v84, 12, v85
	s_waitcnt lgkmcnt(0)
	v_rcp_f32_e32 v66, v66
	v_rcp_f32_e32 v67, v67
	v_rcp_f32_e32 v68, v68
	v_rcp_f32_e32 v69, v69
	v_rcp_f32_e32 v70, v70
	v_rcp_f32_e32 v71, v71
	v_rcp_f32_e32 v72, v72
	v_rcp_f32_e32 v73, v73
	v_rcp_f32_e32 v74, v74
	v_rcp_f32_e32 v75, v75
	v_rcp_f32_e32 v76, v76
	v_rcp_f32_e32 v77, v77
	v_rcp_f32_e32 v78, v78
	v_rcp_f32_e32 v79, v79
	v_rcp_f32_e32 v80, v80
	v_rcp_f32_e32 v81, v81
	v_pk_mul_f32 v[50:51], v[50:51], v[66:67]
	v_pk_mul_f32 v[34:35], v[34:35], v[66:67]
	v_pk_mul_f32 v[18:19], v[18:19], v[66:67]
	v_pk_mul_f32 v[2:3], v[2:3], v[66:67]
	v_mov_b32_dpp v114, v50 quad_perm:[1,0,3,2] row_mask:0xf bank_mask:0xf
	v_mov_b32_dpp v115, v34 quad_perm:[1,0,3,2] row_mask:0xf bank_mask:0xf
	v_mov_b32_dpp v116, v18 quad_perm:[1,0,3,2] row_mask:0xf bank_mask:0xf
	v_mov_b32_dpp v117, v2 quad_perm:[1,0,3,2] row_mask:0xf bank_mask:0xf
	v_mov_b32_dpp v118, v51 quad_perm:[1,0,3,2] row_mask:0xf bank_mask:0xf
	v_mov_b32_dpp v119, v35 quad_perm:[1,0,3,2] row_mask:0xf bank_mask:0xf
	v_mov_b32_dpp v120, v19 quad_perm:[1,0,3,2] row_mask:0xf bank_mask:0xf
	v_mov_b32_dpp v121, v3 quad_perm:[1,0,3,2] row_mask:0xf bank_mask:0xf
	v_cvt_pk_bf16_f32 v50, v50, v114
	v_cvt_pk_bf16_f32 v34, v34, v115
	v_cvt_pk_bf16_f32 v18, v18, v116
	v_cvt_pk_bf16_f32 v2, v2, v117
	v_cvt_pk_bf16_f32 v51, v51, v118
	v_cvt_pk_bf16_f32 v35, v35, v119
	v_cvt_pk_bf16_f32 v19, v19, v120
	v_cvt_pk_bf16_f32 v3, v3, v121
	v_pk_mul_f32 v[52:53], v[52:53], v[68:69]
	v_pk_mul_f32 v[36:37], v[36:37], v[68:69]
	v_pk_mul_f32 v[20:21], v[20:21], v[68:69]
	v_pk_mul_f32 v[4:5], v[4:5], v[68:69]
	v_mov_b32_dpp v114, v52 quad_perm:[1,0,3,2] row_mask:0xf bank_mask:0xf
	v_mov_b32_dpp v115, v36 quad_perm:[1,0,3,2] row_mask:0xf bank_mask:0xf
	v_mov_b32_dpp v116, v20 quad_perm:[1,0,3,2] row_mask:0xf bank_mask:0xf
	v_mov_b32_dpp v117, v4 quad_perm:[1,0,3,2] row_mask:0xf bank_mask:0xf
	v_mov_b32_dpp v118, v53 quad_perm:[1,0,3,2] row_mask:0xf bank_mask:0xf
	v_mov_b32_dpp v119, v37 quad_perm:[1,0,3,2] row_mask:0xf bank_mask:0xf
	v_mov_b32_dpp v120, v21 quad_perm:[1,0,3,2] row_mask:0xf bank_mask:0xf
	v_mov_b32_dpp v121, v5 quad_perm:[1,0,3,2] row_mask:0xf bank_mask:0xf
	v_cvt_pk_bf16_f32 v52, v52, v114
	v_cvt_pk_bf16_f32 v36, v36, v115
	v_cvt_pk_bf16_f32 v20, v20, v116
	v_cvt_pk_bf16_f32 v4, v4, v117
	v_cvt_pk_bf16_f32 v53, v53, v118
	v_cvt_pk_bf16_f32 v37, v37, v119
	v_cvt_pk_bf16_f32 v21, v21, v120
	v_cvt_pk_bf16_f32 v5, v5, v121
	v_pk_mul_f32 v[54:55], v[54:55], v[70:71]
	v_pk_mul_f32 v[38:39], v[38:39], v[70:71]
	v_pk_mul_f32 v[22:23], v[22:23], v[70:71]
	v_pk_mul_f32 v[6:7], v[6:7], v[70:71]
	v_mov_b32_dpp v114, v54 quad_perm:[1,0,3,2] row_mask:0xf bank_mask:0xf
	v_mov_b32_dpp v115, v38 quad_perm:[1,0,3,2] row_mask:0xf bank_mask:0xf
	v_mov_b32_dpp v116, v22 quad_perm:[1,0,3,2] row_mask:0xf bank_mask:0xf
	v_mov_b32_dpp v117, v6 quad_perm:[1,0,3,2] row_mask:0xf bank_mask:0xf
	v_mov_b32_dpp v118, v55 quad_perm:[1,0,3,2] row_mask:0xf bank_mask:0xf
	v_mov_b32_dpp v119, v39 quad_perm:[1,0,3,2] row_mask:0xf bank_mask:0xf
	v_mov_b32_dpp v120, v23 quad_perm:[1,0,3,2] row_mask:0xf bank_mask:0xf
	v_mov_b32_dpp v121, v7 quad_perm:[1,0,3,2] row_mask:0xf bank_mask:0xf
	v_cvt_pk_bf16_f32 v54, v54, v114
	v_cvt_pk_bf16_f32 v38, v38, v115
	v_cvt_pk_bf16_f32 v22, v22, v116
	v_cvt_pk_bf16_f32 v6, v6, v117
	v_cvt_pk_bf16_f32 v55, v55, v118
	v_cvt_pk_bf16_f32 v39, v39, v119
	v_cvt_pk_bf16_f32 v23, v23, v120
	v_cvt_pk_bf16_f32 v7, v7, v121
	v_pk_mul_f32 v[56:57], v[56:57], v[72:73]
	v_pk_mul_f32 v[40:41], v[40:41], v[72:73]
	v_pk_mul_f32 v[24:25], v[24:25], v[72:73]
	v_pk_mul_f32 v[8:9], v[8:9], v[72:73]
	v_mov_b32_dpp v114, v56 quad_perm:[1,0,3,2] row_mask:0xf bank_mask:0xf
	v_mov_b32_dpp v115, v40 quad_perm:[1,0,3,2] row_mask:0xf bank_mask:0xf
	v_mov_b32_dpp v116, v24 quad_perm:[1,0,3,2] row_mask:0xf bank_mask:0xf
	v_mov_b32_dpp v117, v8 quad_perm:[1,0,3,2] row_mask:0xf bank_mask:0xf
	v_mov_b32_dpp v118, v57 quad_perm:[1,0,3,2] row_mask:0xf bank_mask:0xf
	v_mov_b32_dpp v119, v41 quad_perm:[1,0,3,2] row_mask:0xf bank_mask:0xf
	v_mov_b32_dpp v120, v25 quad_perm:[1,0,3,2] row_mask:0xf bank_mask:0xf
	v_mov_b32_dpp v121, v9 quad_perm:[1,0,3,2] row_mask:0xf bank_mask:0xf
	v_cvt_pk_bf16_f32 v56, v56, v114
	v_cvt_pk_bf16_f32 v40, v40, v115
	v_cvt_pk_bf16_f32 v24, v24, v116
	v_cvt_pk_bf16_f32 v8, v8, v117
	v_cvt_pk_bf16_f32 v57, v57, v118
	v_cvt_pk_bf16_f32 v41, v41, v119
	v_cvt_pk_bf16_f32 v25, v25, v120
	v_cvt_pk_bf16_f32 v9, v9, v121
	v_pk_mul_f32 v[58:59], v[58:59], v[74:75]
	v_pk_mul_f32 v[42:43], v[42:43], v[74:75]
	v_pk_mul_f32 v[26:27], v[26:27], v[74:75]
	v_pk_mul_f32 v[10:11], v[10:11], v[74:75]
	v_mov_b32_dpp v114, v58 quad_perm:[1,0,3,2] row_mask:0xf bank_mask:0xf
	v_mov_b32_dpp v115, v42 quad_perm:[1,0,3,2] row_mask:0xf bank_mask:0xf
	v_mov_b32_dpp v116, v26 quad_perm:[1,0,3,2] row_mask:0xf bank_mask:0xf
	v_mov_b32_dpp v117, v10 quad_perm:[1,0,3,2] row_mask:0xf bank_mask:0xf
	v_mov_b32_dpp v118, v59 quad_perm:[1,0,3,2] row_mask:0xf bank_mask:0xf
	v_mov_b32_dpp v119, v43 quad_perm:[1,0,3,2] row_mask:0xf bank_mask:0xf
	v_mov_b32_dpp v120, v27 quad_perm:[1,0,3,2] row_mask:0xf bank_mask:0xf
	v_mov_b32_dpp v121, v11 quad_perm:[1,0,3,2] row_mask:0xf bank_mask:0xf
	v_cvt_pk_bf16_f32 v58, v58, v114
	v_cvt_pk_bf16_f32 v42, v42, v115
	v_cvt_pk_bf16_f32 v26, v26, v116
	v_cvt_pk_bf16_f32 v10, v10, v117
	v_cvt_pk_bf16_f32 v59, v59, v118
	v_cvt_pk_bf16_f32 v43, v43, v119
	v_cvt_pk_bf16_f32 v27, v27, v120
	v_cvt_pk_bf16_f32 v11, v11, v121
	v_pk_mul_f32 v[60:61], v[60:61], v[76:77]
	v_pk_mul_f32 v[44:45], v[44:45], v[76:77]
	v_pk_mul_f32 v[28:29], v[28:29], v[76:77]
	v_pk_mul_f32 v[12:13], v[12:13], v[76:77]
	v_mov_b32_dpp v114, v60 quad_perm:[1,0,3,2] row_mask:0xf bank_mask:0xf
	v_mov_b32_dpp v115, v44 quad_perm:[1,0,3,2] row_mask:0xf bank_mask:0xf
	v_mov_b32_dpp v116, v28 quad_perm:[1,0,3,2] row_mask:0xf bank_mask:0xf
	v_mov_b32_dpp v117, v12 quad_perm:[1,0,3,2] row_mask:0xf bank_mask:0xf
	v_mov_b32_dpp v118, v61 quad_perm:[1,0,3,2] row_mask:0xf bank_mask:0xf
	v_mov_b32_dpp v119, v45 quad_perm:[1,0,3,2] row_mask:0xf bank_mask:0xf
	v_mov_b32_dpp v120, v29 quad_perm:[1,0,3,2] row_mask:0xf bank_mask:0xf
	v_mov_b32_dpp v121, v13 quad_perm:[1,0,3,2] row_mask:0xf bank_mask:0xf
	v_cvt_pk_bf16_f32 v60, v60, v114
	v_cvt_pk_bf16_f32 v44, v44, v115
	v_cvt_pk_bf16_f32 v28, v28, v116
	v_cvt_pk_bf16_f32 v12, v12, v117
	v_cvt_pk_bf16_f32 v61, v61, v118
	v_cvt_pk_bf16_f32 v45, v45, v119
	v_cvt_pk_bf16_f32 v29, v29, v120
	v_cvt_pk_bf16_f32 v13, v13, v121
	v_pk_mul_f32 v[62:63], v[62:63], v[78:79]
	v_pk_mul_f32 v[46:47], v[46:47], v[78:79]
	v_pk_mul_f32 v[30:31], v[30:31], v[78:79]
	v_pk_mul_f32 v[14:15], v[14:15], v[78:79]
	v_mov_b32_dpp v114, v62 quad_perm:[1,0,3,2] row_mask:0xf bank_mask:0xf
	v_mov_b32_dpp v115, v46 quad_perm:[1,0,3,2] row_mask:0xf bank_mask:0xf
	v_mov_b32_dpp v116, v30 quad_perm:[1,0,3,2] row_mask:0xf bank_mask:0xf
	v_mov_b32_dpp v117, v14 quad_perm:[1,0,3,2] row_mask:0xf bank_mask:0xf
	v_mov_b32_dpp v118, v63 quad_perm:[1,0,3,2] row_mask:0xf bank_mask:0xf
	v_mov_b32_dpp v119, v47 quad_perm:[1,0,3,2] row_mask:0xf bank_mask:0xf
	v_mov_b32_dpp v120, v31 quad_perm:[1,0,3,2] row_mask:0xf bank_mask:0xf
	v_mov_b32_dpp v121, v15 quad_perm:[1,0,3,2] row_mask:0xf bank_mask:0xf
	v_cvt_pk_bf16_f32 v62, v62, v114
	v_cvt_pk_bf16_f32 v46, v46, v115
	v_cvt_pk_bf16_f32 v30, v30, v116
	v_cvt_pk_bf16_f32 v14, v14, v117
	v_cvt_pk_bf16_f32 v63, v63, v118
	v_cvt_pk_bf16_f32 v47, v47, v119
	v_cvt_pk_bf16_f32 v31, v31, v120
	v_cvt_pk_bf16_f32 v15, v15, v121
	v_pk_mul_f32 v[64:65], v[64:65], v[80:81]
	v_pk_mul_f32 v[48:49], v[48:49], v[80:81]
	v_pk_mul_f32 v[32:33], v[32:33], v[80:81]
	v_pk_mul_f32 v[16:17], v[16:17], v[80:81]
	v_mov_b32_dpp v114, v64 quad_perm:[1,0,3,2] row_mask:0xf bank_mask:0xf
	v_mov_b32_dpp v115, v48 quad_perm:[1,0,3,2] row_mask:0xf bank_mask:0xf
	v_mov_b32_dpp v116, v32 quad_perm:[1,0,3,2] row_mask:0xf bank_mask:0xf
	v_mov_b32_dpp v117, v16 quad_perm:[1,0,3,2] row_mask:0xf bank_mask:0xf
	v_mov_b32_dpp v118, v65 quad_perm:[1,0,3,2] row_mask:0xf bank_mask:0xf
	v_mov_b32_dpp v119, v49 quad_perm:[1,0,3,2] row_mask:0xf bank_mask:0xf
	v_mov_b32_dpp v120, v33 quad_perm:[1,0,3,2] row_mask:0xf bank_mask:0xf
	v_mov_b32_dpp v121, v17 quad_perm:[1,0,3,2] row_mask:0xf bank_mask:0xf
	v_cvt_pk_bf16_f32 v64, v64, v114
	v_cvt_pk_bf16_f32 v48, v48, v115
	v_cvt_pk_bf16_f32 v32, v32, v116
	v_cvt_pk_bf16_f32 v16, v16, v117
	v_cvt_pk_bf16_f32 v65, v65, v118
	v_cvt_pk_bf16_f32 v49, v49, v119
	v_cvt_pk_bf16_f32 v33, v33, v120
	v_cvt_pk_bf16_f32 v17, v17, v121
	s_mov_b64 s[100:101], exec
	s_and_b64 exec, exec, s[6:7]
	ds_write_b32 v83, v50
	ds_write_b32 v83, v34 offset:64
	ds_write_b32 v83, v18 offset:128
	ds_write_b32 v83, v2 offset:192
	ds_write_b32 v83, v51 offset:256
	ds_write_b32 v83, v35 offset:320
	ds_write_b32 v83, v19 offset:384
	ds_write_b32 v83, v3 offset:448
	ds_write_b32 v83, v52 offset:512
	ds_write_b32 v83, v36 offset:576
	ds_write_b32 v83, v20 offset:640
	ds_write_b32 v83, v4 offset:704
	ds_write_b32 v83, v53 offset:768
	ds_write_b32 v83, v37 offset:832
	ds_write_b32 v83, v21 offset:896
	ds_write_b32 v83, v5 offset:960
	ds_write_b32 v83, v54 offset:2048
	ds_write_b32 v83, v38 offset:2112
	ds_write_b32 v83, v22 offset:2176
	ds_write_b32 v83, v6 offset:2240
	ds_write_b32 v83, v55 offset:2304
	ds_write_b32 v83, v39 offset:2368
	ds_write_b32 v83, v23 offset:2432
	ds_write_b32 v83, v7 offset:2496
	ds_write_b32 v83, v56 offset:2560
	ds_write_b32 v83, v40 offset:2624
	ds_write_b32 v83, v24 offset:2688
	ds_write_b32 v83, v8 offset:2752
	ds_write_b32 v83, v57 offset:2816
	ds_write_b32 v83, v41 offset:2880
	ds_write_b32 v83, v25 offset:2944
	ds_write_b32 v83, v9 offset:3008
	ds_write_b32 v83, v58 offset:4096
	ds_write_b32 v83, v42 offset:4160
	ds_write_b32 v83, v26 offset:4224
	ds_write_b32 v83, v10 offset:4288
	ds_write_b32 v83, v59 offset:4352
	ds_write_b32 v83, v43 offset:4416
	ds_write_b32 v83, v27 offset:4480
	ds_write_b32 v83, v11 offset:4544
	ds_write_b32 v83, v60 offset:4608
	ds_write_b32 v83, v44 offset:4672
	ds_write_b32 v83, v28 offset:4736
	ds_write_b32 v83, v12 offset:4800
	ds_write_b32 v83, v61 offset:4864
	ds_write_b32 v83, v45 offset:4928
	ds_write_b32 v83, v29 offset:4992
	ds_write_b32 v83, v13 offset:5056
	ds_write_b32 v83, v62 offset:6144
	ds_write_b32 v83, v46 offset:6208
	ds_write_b32 v83, v30 offset:6272
	ds_write_b32 v83, v14 offset:6336
	ds_write_b32 v83, v63 offset:6400
	ds_write_b32 v83, v47 offset:6464
	ds_write_b32 v83, v31 offset:6528
	ds_write_b32 v83, v15 offset:6592
	ds_write_b32 v83, v64 offset:6656
	ds_write_b32 v83, v48 offset:6720
	ds_write_b32 v83, v32 offset:6784
	ds_write_b32 v83, v16 offset:6848
	ds_write_b32 v83, v65 offset:6912
	ds_write_b32 v83, v49 offset:6976
	ds_write_b32 v83, v33 offset:7040
	ds_write_b32 v83, v17 offset:7104
	s_mov_b64 exec, s[100:101]
	ds_read_b128 v[66:69], v82
	ds_read_b128 v[70:73], v82 offset:1024
	ds_read_b128 v[74:77], v82 offset:2048
	ds_read_b128 v[78:81], v82 offset:3072
	ds_read_b128 v[86:89], v82 offset:4096
	ds_read_b128 v[90:93], v82 offset:5120
	ds_read_b128 v[94:97], v82 offset:6144
	ds_read_b128 v[98:101], v82 offset:7168
	s_waitcnt lgkmcnt(7)
	global_store_dwordx4 v84, v[66:69], s[0:1] nt
	s_waitcnt lgkmcnt(6)
	v_add_u32_e32 v85, 16384, v84
	global_store_dwordx4 v85, v[70:73], s[0:1] nt
	s_waitcnt lgkmcnt(5)
	v_add_u32_e32 v85, 32768, v84
	global_store_dwordx4 v85, v[74:77], s[0:1] nt
	s_waitcnt lgkmcnt(4)
	v_add_u32_e32 v85, 49152, v84
	global_store_dwordx4 v85, v[78:81], s[0:1] nt
	s_waitcnt lgkmcnt(3)
	v_add_u32_e32 v85, 65536, v84
	global_store_dwordx4 v85, v[86:89], s[0:1] nt
	s_waitcnt lgkmcnt(2)
	v_add_u32_e32 v85, 81920, v84
	global_store_dwordx4 v85, v[90:93], s[0:1] nt
	s_waitcnt lgkmcnt(1)
	v_add_u32_e32 v85, 98304, v84
	global_store_dwordx4 v85, v[94:97], s[0:1] nt
	s_waitcnt lgkmcnt(0)
	v_add_u32_e32 v85, 114688, v84
	global_store_dwordx4 v85, v[98:101], s[0:1] nt
	s_branch .LBB0_593

.LBB0_862:
	s_waitcnt vmcnt(8)
	s_waitcnt vmcnt(9)
	ds_write_b128 v222, v[98:101] offset:32768
	s_waitcnt vmcnt(8)
	ds_write_b128 v222, v[102:105] offset:40960
	s_and_saveexec_b64 s[8:9], s[4:5]
	ds_write_b32 v224, v114
	s_or_b64 exec, exec, s[8:9]
	s_waitcnt lgkmcnt(0)
	ds_read_b128 v[66:69], v205
	ds_read_b128 v[70:73], v205 offset:32
	ds_read_b128 v[74:77], v205 offset:64
	ds_read_b128 v[78:81], v205 offset:96
	s_add_u32 s0, s26, s28
	s_addc_u32 s1, s27, s29
	s_lshl_b32 s2, s47, 12
	s_add_u32 s0, s0, s2
	s_addc_u32 s1, s1, 0
	v_lshrrev_b32_e32 v82, 6, v254
	v_lshlrev_b32_e32 v82, 13, v82
	v_add_u32_e32 v82, 0x11000, v82
	v_and_b32_e32 v83, 31, v214
	v_lshrrev_b32_e32 v84, 5, v214
	v_lshlrev_b32_e32 v83, 1, v83
	v_lshl_add_u32 v83, v84, 10, v83
	v_add_u32_e32 v83, v82, v83
	v_lshl_add_u32 v82, v214, 4, v82
	v_lshrrev_b32_e32 v84, 4, v214
	v_and_b32_e32 v85, 15, v214
	v_lshlrev_b32_e32 v85, 4, v85
	v_lshl_add_u32 v84, v84, 12, v85
	s_waitcnt lgkmcnt(0)
	v_rcp_f32_e32 v66, v66
	v_rcp_f32_e32 v67, v67
	v_rcp_f32_e32 v68, v68
	v_rcp_f32_e32 v69, v69
	v_rcp_f32_e32 v70, v70
	v_rcp_f32_e32 v71, v71
	v_rcp_f32_e32 v72, v72
	v_rcp_f32_e32 v73, v73
	v_rcp_f32_e32 v74, v74
	v_rcp_f32_e32 v75, v75
	v_rcp_f32_e32 v76, v76
	v_rcp_f32_e32 v77, v77
	v_rcp_f32_e32 v78, v78
	v_rcp_f32_e32 v79, v79
	v_rcp_f32_e32 v80, v80
	v_rcp_f32_e32 v81, v81
	v_pk_mul_f32 v[50:51], v[50:51], v[66:67]
	v_pk_mul_f32 v[34:35], v[34:35], v[66:67]
	v_pk_mul_f32 v[18:19], v[18:19], v[66:67]
	v_pk_mul_f32 v[2:3], v[2:3], v[66:67]
	v_mov_b32_dpp v114, v50 quad_perm:[1,0,3,2] row_mask:0xf bank_mask:0xf
	v_mov_b32_dpp v115, v34 quad_perm:[1,0,3,2] row_mask:0xf bank_mask:0xf
	v_mov_b32_dpp v116, v18 quad_perm:[1,0,3,2] row_mask:0xf bank_mask:0xf
	v_mov_b32_dpp v117, v2 quad_perm:[1,0,3,2] row_mask:0xf bank_mask:0xf
	v_mov_b32_dpp v118, v51 quad_perm:[1,0,3,2] row_mask:0xf bank_mask:0xf
	v_mov_b32_dpp v119, v35 quad_perm:[1,0,3,2] row_mask:0xf bank_mask:0xf
	v_mov_b32_dpp v120, v19 quad_perm:[1,0,3,2] row_mask:0xf bank_mask:0xf
	v_mov_b32_dpp v121, v3 quad_perm:[1,0,3,2] row_mask:0xf bank_mask:0xf
	v_cvt_pk_bf16_f32 v50, v50, v114
	v_cvt_pk_bf16_f32 v34, v34, v115
	v_cvt_pk_bf16_f32 v18, v18, v116
	v_cvt_pk_bf16_f32 v2, v2, v117
	v_cvt_pk_bf16_f32 v51, v51, v118
	v_cvt_pk_bf16_f32 v35, v35, v119
	v_cvt_pk_bf16_f32 v19, v19, v120
	v_cvt_pk_bf16_f32 v3, v3, v121
	v_pk_mul_f32 v[52:53], v[52:53], v[68:69]
	v_pk_mul_f32 v[36:37], v[36:37], v[68:69]
	v_pk_mul_f32 v[20:21], v[20:21], v[68:69]
	v_pk_mul_f32 v[4:5], v[4:5], v[68:69]
	v_mov_b32_dpp v114, v52 quad_perm:[1,0,3,2] row_mask:0xf bank_mask:0xf
	v_mov_b32_dpp v115, v36 quad_perm:[1,0,3,2] row_mask:0xf bank_mask:0xf
	v_mov_b32_dpp v116, v20 quad_perm:[1,0,3,2] row_mask:0xf bank_mask:0xf
	v_mov_b32_dpp v117, v4 quad_perm:[1,0,3,2] row_mask:0xf bank_mask:0xf
	v_mov_b32_dpp v118, v53 quad_perm:[1,0,3,2] row_mask:0xf bank_mask:0xf
	v_mov_b32_dpp v119, v37 quad_perm:[1,0,3,2] row_mask:0xf bank_mask:0xf
	v_mov_b32_dpp v120, v21 quad_perm:[1,0,3,2] row_mask:0xf bank_mask:0xf
	v_mov_b32_dpp v121, v5 quad_perm:[1,0,3,2] row_mask:0xf bank_mask:0xf
	v_cvt_pk_bf16_f32 v52, v52, v114
	v_cvt_pk_bf16_f32 v36, v36, v115
	v_cvt_pk_bf16_f32 v20, v20, v116
	v_cvt_pk_bf16_f32 v4, v4, v117
	v_cvt_pk_bf16_f32 v53, v53, v118
	v_cvt_pk_bf16_f32 v37, v37, v119
	v_cvt_pk_bf16_f32 v21, v21, v120
	v_cvt_pk_bf16_f32 v5, v5, v121
	v_pk_mul_f32 v[54:55], v[54:55], v[70:71]
	v_pk_mul_f32 v[38:39], v[38:39], v[70:71]
	v_pk_mul_f32 v[22:23], v[22:23], v[70:71]
	v_pk_mul_f32 v[6:7], v[6:7], v[70:71]
	v_mov_b32_dpp v114, v54 quad_perm:[1,0,3,2] row_mask:0xf bank_mask:0xf
	v_mov_b32_dpp v115, v38 quad_perm:[1,0,3,2] row_mask:0xf bank_mask:0xf
	v_mov_b32_dpp v116, v22 quad_perm:[1,0,3,2] row_mask:0xf bank_mask:0xf
	v_mov_b32_dpp v117, v6 quad_perm:[1,0,3,2] row_mask:0xf bank_mask:0xf
	v_mov_b32_dpp v118, v55 quad_perm:[1,0,3,2] row_mask:0xf bank_mask:0xf
	v_mov_b32_dpp v119, v39 quad_perm:[1,0,3,2] row_mask:0xf bank_mask:0xf
	v_mov_b32_dpp v120, v23 quad_perm:[1,0,3,2] row_mask:0xf bank_mask:0xf
	v_mov_b32_dpp v121, v7 quad_perm:[1,0,3,2] row_mask:0xf bank_mask:0xf
	v_cvt_pk_bf16_f32 v54, v54, v114
	v_cvt_pk_bf16_f32 v38, v38, v115
	v_cvt_pk_bf16_f32 v22, v22, v116
	v_cvt_pk_bf16_f32 v6, v6, v117
	v_cvt_pk_bf16_f32 v55, v55, v118
	v_cvt_pk_bf16_f32 v39, v39, v119
	v_cvt_pk_bf16_f32 v23, v23, v120
	v_cvt_pk_bf16_f32 v7, v7, v121
	v_pk_mul_f32 v[56:57], v[56:57], v[72:73]
	v_pk_mul_f32 v[40:41], v[40:41], v[72:73]
	v_pk_mul_f32 v[24:25], v[24:25], v[72:73]
	v_pk_mul_f32 v[8:9], v[8:9], v[72:73]
	v_mov_b32_dpp v114, v56 quad_perm:[1,0,3,2] row_mask:0xf bank_mask:0xf
	v_mov_b32_dpp v115, v40 quad_perm:[1,0,3,2] row_mask:0xf bank_mask:0xf
	v_mov_b32_dpp v116, v24 quad_perm:[1,0,3,2] row_mask:0xf bank_mask:0xf
	v_mov_b32_dpp v117, v8 quad_perm:[1,0,3,2] row_mask:0xf bank_mask:0xf
	v_mov_b32_dpp v118, v57 quad_perm:[1,0,3,2] row_mask:0xf bank_mask:0xf
	v_mov_b32_dpp v119, v41 quad_perm:[1,0,3,2] row_mask:0xf bank_mask:0xf
	v_mov_b32_dpp v120, v25 quad_perm:[1,0,3,2] row_mask:0xf bank_mask:0xf
	v_mov_b32_dpp v121, v9 quad_perm:[1,0,3,2] row_mask:0xf bank_mask:0xf
	v_cvt_pk_bf16_f32 v56, v56, v114
	v_cvt_pk_bf16_f32 v40, v40, v115
	v_cvt_pk_bf16_f32 v24, v24, v116
	v_cvt_pk_bf16_f32 v8, v8, v117
	v_cvt_pk_bf16_f32 v57, v57, v118
	v_cvt_pk_bf16_f32 v41, v41, v119
	v_cvt_pk_bf16_f32 v25, v25, v120
	v_cvt_pk_bf16_f32 v9, v9, v121
	v_pk_mul_f32 v[58:59], v[58:59], v[74:75]
	v_pk_mul_f32 v[42:43], v[42:43], v[74:75]
	v_pk_mul_f32 v[26:27], v[26:27], v[74:75]
	v_pk_mul_f32 v[10:11], v[10:11], v[74:75]
	v_mov_b32_dpp v114, v58 quad_perm:[1,0,3,2] row_mask:0xf bank_mask:0xf
	v_mov_b32_dpp v115, v42 quad_perm:[1,0,3,2] row_mask:0xf bank_mask:0xf
	v_mov_b32_dpp v116, v26 quad_perm:[1,0,3,2] row_mask:0xf bank_mask:0xf
	v_mov_b32_dpp v117, v10 quad_perm:[1,0,3,2] row_mask:0xf bank_mask:0xf
	v_mov_b32_dpp v118, v59 quad_perm:[1,0,3,2] row_mask:0xf bank_mask:0xf
	v_mov_b32_dpp v119, v43 quad_perm:[1,0,3,2] row_mask:0xf bank_mask:0xf
	v_mov_b32_dpp v120, v27 quad_perm:[1,0,3,2] row_mask:0xf bank_mask:0xf
	v_mov_b32_dpp v121, v11 quad_perm:[1,0,3,2] row_mask:0xf bank_mask:0xf
	v_cvt_pk_bf16_f32 v58, v58, v114
	v_cvt_pk_bf16_f32 v42, v42, v115
	v_cvt_pk_bf16_f32 v26, v26, v116
	v_cvt_pk_bf16_f32 v10, v10, v117
	v_cvt_pk_bf16_f32 v59, v59, v118
	v_cvt_pk_bf16_f32 v43, v43, v119
	v_cvt_pk_bf16_f32 v27, v27, v120
	v_cvt_pk_bf16_f32 v11, v11, v121
	v_pk_mul_f32 v[60:61], v[60:61], v[76:77]
	v_pk_mul_f32 v[44:45], v[44:45], v[76:77]
	v_pk_mul_f32 v[28:29], v[28:29], v[76:77]
	v_pk_mul_f32 v[12:13], v[12:13], v[76:77]
	v_mov_b32_dpp v114, v60 quad_perm:[1,0,3,2] row_mask:0xf bank_mask:0xf
	v_mov_b32_dpp v115, v44 quad_perm:[1,0,3,2] row_mask:0xf bank_mask:0xf
	v_mov_b32_dpp v116, v28 quad_perm:[1,0,3,2] row_mask:0xf bank_mask:0xf
	v_mov_b32_dpp v117, v12 quad_perm:[1,0,3,2] row_mask:0xf bank_mask:0xf
	v_mov_b32_dpp v118, v61 quad_perm:[1,0,3,2] row_mask:0xf bank_mask:0xf
	v_mov_b32_dpp v119, v45 quad_perm:[1,0,3,2] row_mask:0xf bank_mask:0xf
	v_mov_b32_dpp v120, v29 quad_perm:[1,0,3,2] row_mask:0xf bank_mask:0xf
	v_mov_b32_dpp v121, v13 quad_perm:[1,0,3,2] row_mask:0xf bank_mask:0xf
	v_cvt_pk_bf16_f32 v60, v60, v114
	v_cvt_pk_bf16_f32 v44, v44, v115
	v_cvt_pk_bf16_f32 v28, v28, v116
	v_cvt_pk_bf16_f32 v12, v12, v117
	v_cvt_pk_bf16_f32 v61, v61, v118
	v_cvt_pk_bf16_f32 v45, v45, v119
	v_cvt_pk_bf16_f32 v29, v29, v120
	v_cvt_pk_bf16_f32 v13, v13, v121
	v_pk_mul_f32 v[62:63], v[62:63], v[78:79]
	v_pk_mul_f32 v[46:47], v[46:47], v[78:79]
	v_pk_mul_f32 v[30:31], v[30:31], v[78:79]
	v_pk_mul_f32 v[14:15], v[14:15], v[78:79]
	v_mov_b32_dpp v114, v62 quad_perm:[1,0,3,2] row_mask:0xf bank_mask:0xf
	v_mov_b32_dpp v115, v46 quad_perm:[1,0,3,2] row_mask:0xf bank_mask:0xf
	v_mov_b32_dpp v116, v30 quad_perm:[1,0,3,2] row_mask:0xf bank_mask:0xf
	v_mov_b32_dpp v117, v14 quad_perm:[1,0,3,2] row_mask:0xf bank_mask:0xf
	v_mov_b32_dpp v118, v63 quad_perm:[1,0,3,2] row_mask:0xf bank_mask:0xf
	v_mov_b32_dpp v119, v47 quad_perm:[1,0,3,2] row_mask:0xf bank_mask:0xf
	v_mov_b32_dpp v120, v31 quad_perm:[1,0,3,2] row_mask:0xf bank_mask:0xf
	v_mov_b32_dpp v121, v15 quad_perm:[1,0,3,2] row_mask:0xf bank_mask:0xf
	v_cvt_pk_bf16_f32 v62, v62, v114
	v_cvt_pk_bf16_f32 v46, v46, v115
	v_cvt_pk_bf16_f32 v30, v30, v116
	v_cvt_pk_bf16_f32 v14, v14, v117
	v_cvt_pk_bf16_f32 v63, v63, v118
	v_cvt_pk_bf16_f32 v47, v47, v119
	v_cvt_pk_bf16_f32 v31, v31, v120
	v_cvt_pk_bf16_f32 v15, v15, v121
	v_pk_mul_f32 v[64:65], v[64:65], v[80:81]
	v_pk_mul_f32 v[48:49], v[48:49], v[80:81]
	v_pk_mul_f32 v[32:33], v[32:33], v[80:81]
	v_pk_mul_f32 v[16:17], v[16:17], v[80:81]
	v_mov_b32_dpp v114, v64 quad_perm:[1,0,3,2] row_mask:0xf bank_mask:0xf
	v_mov_b32_dpp v115, v48 quad_perm:[1,0,3,2] row_mask:0xf bank_mask:0xf
	v_mov_b32_dpp v116, v32 quad_perm:[1,0,3,2] row_mask:0xf bank_mask:0xf
	v_mov_b32_dpp v117, v16 quad_perm:[1,0,3,2] row_mask:0xf bank_mask:0xf
	v_mov_b32_dpp v118, v65 quad_perm:[1,0,3,2] row_mask:0xf bank_mask:0xf
	v_mov_b32_dpp v119, v49 quad_perm:[1,0,3,2] row_mask:0xf bank_mask:0xf
	v_mov_b32_dpp v120, v33 quad_perm:[1,0,3,2] row_mask:0xf bank_mask:0xf
	v_mov_b32_dpp v121, v17 quad_perm:[1,0,3,2] row_mask:0xf bank_mask:0xf
	v_cvt_pk_bf16_f32 v64, v64, v114
	v_cvt_pk_bf16_f32 v48, v48, v115
	v_cvt_pk_bf16_f32 v32, v32, v116
	v_cvt_pk_bf16_f32 v16, v16, v117
	v_cvt_pk_bf16_f32 v65, v65, v118
	v_cvt_pk_bf16_f32 v49, v49, v119
	v_cvt_pk_bf16_f32 v33, v33, v120
	v_cvt_pk_bf16_f32 v17, v17, v121
	s_mov_b64 s[100:101], exec
	s_and_b64 exec, exec, s[6:7]
	ds_write_b32 v83, v50
	ds_write_b32 v83, v34 offset:64
	ds_write_b32 v83, v18 offset:128
	ds_write_b32 v83, v2 offset:192
	ds_write_b32 v83, v51 offset:256
	ds_write_b32 v83, v35 offset:320
	ds_write_b32 v83, v19 offset:384
	ds_write_b32 v83, v3 offset:448
	ds_write_b32 v83, v52 offset:512
	ds_write_b32 v83, v36 offset:576
	ds_write_b32 v83, v20 offset:640
	ds_write_b32 v83, v4 offset:704
	ds_write_b32 v83, v53 offset:768
	ds_write_b32 v83, v37 offset:832
	ds_write_b32 v83, v21 offset:896
	ds_write_b32 v83, v5 offset:960
	ds_write_b32 v83, v54 offset:2048
	ds_write_b32 v83, v38 offset:2112
	ds_write_b32 v83, v22 offset:2176
	ds_write_b32 v83, v6 offset:2240
	ds_write_b32 v83, v55 offset:2304
	ds_write_b32 v83, v39 offset:2368
	ds_write_b32 v83, v23 offset:2432
	ds_write_b32 v83, v7 offset:2496
	ds_write_b32 v83, v56 offset:2560
	ds_write_b32 v83, v40 offset:2624
	ds_write_b32 v83, v24 offset:2688
	ds_write_b32 v83, v8 offset:2752
	ds_write_b32 v83, v57 offset:2816
	ds_write_b32 v83, v41 offset:2880
	ds_write_b32 v83, v25 offset:2944
	ds_write_b32 v83, v9 offset:3008
	ds_write_b32 v83, v58 offset:4096
	ds_write_b32 v83, v42 offset:4160
	ds_write_b32 v83, v26 offset:4224
	ds_write_b32 v83, v10 offset:4288
	ds_write_b32 v83, v59 offset:4352
	ds_write_b32 v83, v43 offset:4416
	ds_write_b32 v83, v27 offset:4480
	ds_write_b32 v83, v11 offset:4544
	ds_write_b32 v83, v60 offset:4608
	ds_write_b32 v83, v44 offset:4672
	ds_write_b32 v83, v28 offset:4736
	ds_write_b32 v83, v12 offset:4800
	ds_write_b32 v83, v61 offset:4864
	ds_write_b32 v83, v45 offset:4928
	ds_write_b32 v83, v29 offset:4992
	ds_write_b32 v83, v13 offset:5056
	ds_write_b32 v83, v62 offset:6144
	ds_write_b32 v83, v46 offset:6208
	ds_write_b32 v83, v30 offset:6272
	ds_write_b32 v83, v14 offset:6336
	ds_write_b32 v83, v63 offset:6400
	ds_write_b32 v83, v47 offset:6464
	ds_write_b32 v83, v31 offset:6528
	ds_write_b32 v83, v15 offset:6592
	ds_write_b32 v83, v64 offset:6656
	ds_write_b32 v83, v48 offset:6720
	ds_write_b32 v83, v32 offset:6784
	ds_write_b32 v83, v16 offset:6848
	ds_write_b32 v83, v65 offset:6912
	ds_write_b32 v83, v49 offset:6976
	ds_write_b32 v83, v33 offset:7040
	ds_write_b32 v83, v17 offset:7104
	s_mov_b64 exec, s[100:101]
	ds_read_b128 v[66:69], v82
	ds_read_b128 v[70:73], v82 offset:1024
	ds_read_b128 v[74:77], v82 offset:2048
	ds_read_b128 v[78:81], v82 offset:3072
	ds_read_b128 v[86:89], v82 offset:4096
	ds_read_b128 v[90:93], v82 offset:5120
	ds_read_b128 v[94:97], v82 offset:6144
	ds_read_b128 v[98:101], v82 offset:7168
	s_waitcnt lgkmcnt(7)
	global_store_dwordx4 v84, v[66:69], s[0:1] nt
	s_waitcnt lgkmcnt(6)
	v_add_u32_e32 v85, 16384, v84
	global_store_dwordx4 v85, v[70:73], s[0:1] nt
	s_waitcnt lgkmcnt(5)
	v_add_u32_e32 v85, 32768, v84
	global_store_dwordx4 v85, v[74:77], s[0:1] nt
	s_waitcnt lgkmcnt(4)
	v_add_u32_e32 v85, 49152, v84
	global_store_dwordx4 v85, v[78:81], s[0:1] nt
	s_waitcnt lgkmcnt(3)
	v_add_u32_e32 v85, 65536, v84
	global_store_dwordx4 v85, v[86:89], s[0:1] nt
	s_waitcnt lgkmcnt(2)
	v_add_u32_e32 v85, 81920, v84
	global_store_dwordx4 v85, v[90:93], s[0:1] nt
	s_waitcnt lgkmcnt(1)
	v_add_u32_e32 v85, 98304, v84
	global_store_dwordx4 v85, v[94:97], s[0:1] nt
	s_waitcnt lgkmcnt(0)
	v_add_u32_e32 v85, 114688, v84
	global_store_dwordx4 v85, v[98:101], s[0:1] nt
	s_branch .LBB0_819
